# baseline (speedup 1.0000x reference)
.LBB0_32:
	s_or_b64 exec, exec, s[2:3]
	v_mov_b32_e32 v2, s8
	v_lshrrev_b32_e32 v106, 4, v1
	ds_read_b128 v[4:7], v2
	v_lshl_add_u32 v2, v106, 2, s7
	ds_read2_b32 v[14:15], v2 offset1:4
	v_mov_b32_e32 v9, s8
	ds_read_b32 v9, v9 offset:16
	v_and_b32_e32 v83, 48, v0
	v_lshl_add_u32 v64, v83, 2, s6
	ds_read_b128 v[28:31], v64
	v_mov_b32_e32 v2, 0
	v_cmp_ne_u32_e64 s[16:17], 3, v106
	s_waitcnt lgkmcnt(0)
	v_readfirstlane_b32 s35, v4
	v_readfirstlane_b32 s36, v5
	v_mov_b32_e32 v3, v2
	v_mov_b32_e32 v4, v2
	v_mov_b32_e32 v5, v2
	v_lshlrev_b32_e32 v107, 4, v82
	s_and_saveexec_b64 s[4:5], s[16:17]
	s_cbranch_execz .LBB0_34
	v_mov_b32_e32 v4, s14
	v_mov_b32_e32 v5, s26
	v_cmp_eq_u32_e32 vcc, 1, v106
	v_mov_b32_e32 v8, s27
	v_cmp_gt_u32_e64 s[2:3], 16, v1
	v_cndmask_b32_e32 v4, v4, v5, vcc
	v_mov_b32_e32 v5, s15
	v_cndmask_b32_e32 v5, v5, v8, vcc
	v_mov_b32_e32 v8, s25
	s_waitcnt lgkmcnt(0)
	v_cndmask_b32_e32 v3, v9, v7, vcc
	v_cndmask_b32_e64 v5, v5, v8, s[2:3]
	v_mov_b32_e32 v8, s24
	v_cndmask_b32_e64 v3, v3, v6, s[2:3]
	v_lshlrev_b32_e32 v6, 4, v82
	v_cndmask_b32_e64 v4, v4, v8, s[2:3]
	v_lshl_or_b32 v6, v3, 8, v6
	v_mov_b32_e32 v7, v2
	v_lshl_add_u64 v[2:3], v[4:5], 0, v[6:7]
	global_load_dwordx4 v[2:5], v[2:3], off sc0 nt

.LBB0_40:
	s_or_b64 exec, exec, s[2:3]
	v_mov_b32_e32 v18, 0
	v_mov_b32_e32 v19, v18
	v_mov_b32_e32 v20, v18
	v_mov_b32_e32 v21, v18
	v_mov_b64_e32 v[14:15], v[18:19]
	v_cmp_gt_i32_e32 vcc, s35, v106
	v_mov_b64_e32 v[16:17], v[20:21]
	s_and_saveexec_b64 s[2:3], vcc
	s_cbranch_execz .LBB0_42
	s_waitcnt lgkmcnt(0)
	v_lshl_or_b32 v14, v28, 8, v107
	global_load_dwordx4 v[14:17], v14, s[28:29] sc0 nt
